# stack on v55: K/V staging behind the QK block + shortened lazy-rescale test
# speedup vs baseline: 1.0108x; 1.0094x over previous
; DEV void partialSM(f32x16& p0, f32x16& p1, float& m_reg, float& mn, float& alpha) {
;   constexpr float C = SCALE * 1.4426950408889634f;
;   float pmax = p0[0];
; #pragma unroll
;   for (int r = 1; r < 16; ++r) pmax = fmaxf(pmax, p0[r]);
; #pragma unroll
;   for (int r = 0; r < 16; ++r) pmax = fmaxf(pmax, p1[r]);
;   { auto rr = __builtin_amdgcn_permlane32_swap(__float_as_uint(pmax), __float_as_uint(pmax), false, false);
;     pmax = fmaxf(__uint_as_float(rr[0]), __uint_as_float(rr[1])); }
;   if (__builtin_expect(__all(pmax - m_reg <= THR / SCALE), 1)) { mn = m_reg; alpha = 1.f; }
;   else { mn = fmaxf(m_reg, pmax); alpha = __builtin_amdgcn_exp2f((m_reg - mn) * C); m_reg = mn; }
.Lmv2_a:
	s_nop 8
	v_max_f32_e32 v66, v85, v85
	v_max_f32_e32 v219, v84, v84
	v_max_f32_e32 v66, v219, v66
	v_max3_f32 v66, v66, v86, v87
	v_max3_f32 v66, v66, v88, v89
	v_max3_f32 v66, v66, v90, v91
	v_max3_f32 v66, v66, v92, v93
	v_max3_f32 v66, v66, v94, v95
	v_max3_f32 v66, v66, v96, v97
	v_max3_f32 v66, v66, v98, v99
	v_max3_f32 v66, v66, v68, v69
	v_max3_f32 v66, v66, v70, v71
	v_max3_f32 v66, v66, v72, v73
	v_max3_f32 v66, v66, v74, v75
	v_max3_f32 v66, v66, v76, v77
	v_max3_f32 v66, v66, v78, v79
	v_max3_f32 v66, v66, v80, v81
	v_max3_f32 v66, v66, v82, v83
	v_mov_b32_e32 v219, v66
	s_nop 1
	v_permlane32_swap_b32_e32 v66, v219
	v_max_f32_e32 v219, v219, v219
	v_max_f32_e32 v66, v66, v66
	v_max_f32_e32 v66, v66, v219
	v_sub_f32_e32 v219, v66, v215
	v_cmp_ge_f32_e32 vcc, s31, v219
	s_cmp_eq_u64 vcc, exec
	s_cbranch_scc0 .Lresc_a
	v_mov_b32_e32 v219, 1.0
	s_branch .Lnor_a

; DEV void partialSM(f32x16& p0, f32x16& p1, float& m_reg, float& mn, float& alpha) {
;   constexpr float C = SCALE * 1.4426950408889634f;
;   float pmax = p0[0];
; #pragma unroll
;   for (int r = 1; r < 16; ++r) pmax = fmaxf(pmax, p0[r]);
; #pragma unroll
;   for (int r = 0; r < 16; ++r) pmax = fmaxf(pmax, p1[r]);
;   { auto rr = __builtin_amdgcn_permlane32_swap(__float_as_uint(pmax), __float_as_uint(pmax), false, false);
;     pmax = fmaxf(__uint_as_float(rr[0]), __uint_as_float(rr[1])); }
;   if (__builtin_expect(__all(pmax - m_reg <= THR / SCALE), 1)) { mn = m_reg; alpha = 1.f; }
;   else { mn = fmaxf(m_reg, pmax); alpha = __builtin_amdgcn_exp2f((m_reg - mn) * C); m_reg = mn; }
.Lmv2_b:
	s_nop 8
	v_max_f32_e32 v66, v85, v85
	v_max_f32_e32 v219, v84, v84
	v_max_f32_e32 v66, v219, v66
	v_max3_f32 v66, v66, v86, v87
	v_max3_f32 v66, v66, v88, v89
	v_max3_f32 v66, v66, v90, v91
	v_max3_f32 v66, v66, v92, v93
	v_max3_f32 v66, v66, v94, v95
	v_max3_f32 v66, v66, v96, v97
	v_max3_f32 v66, v66, v98, v99
	v_max3_f32 v66, v66, v68, v69
	v_max3_f32 v66, v66, v70, v71
	v_max3_f32 v66, v66, v72, v73
	v_max3_f32 v66, v66, v74, v75
	v_max3_f32 v66, v66, v76, v77
	v_max3_f32 v66, v66, v78, v79
	v_max3_f32 v66, v66, v80, v81
	v_max3_f32 v66, v66, v82, v83
	v_mov_b32_e32 v219, v66
	s_nop 1
	v_permlane32_swap_b32_e32 v66, v219
	v_max_f32_e32 v219, v219, v219
	v_max_f32_e32 v66, v66, v66
	v_max_f32_e32 v66, v66, v219
	v_sub_f32_e32 v219, v66, v215
	v_cmp_ge_f32_e32 vcc, s34, v219
	s_cmp_eq_u64 vcc, exec
	s_cbranch_scc0 .Lresc_b
	v_mov_b32_e32 v219, 1.0
	s_branch .Lnor_b
